# baseline (speedup 1.0000x reference)
.Lq_dma_loop:
	s_lshl_b32 s40, s38, 10
	s_add_u32 s42, s36, s40
	s_addc_u32 s43, s37, 0
	s_add_i32 s41, s40, 69680
	v_lshl_add_u64 v[114:115], s[42:43], 0, v[116:117]
	s_mov_b32 m0, s41
	s_add_i32 s38, s38, 14
	global_load_lds_dwordx4 v[114:115], off
	s_cmp_lt_u32 s38, 64
	s_cbranch_scc1 .Lq_dma_loop

.LBB1_137:
	s_or_b64 exec, exec, s[6:7]
	v_readfirstlane_b32 s10, v0
	s_cmp_ge_i32 s10, s28
	s_mov_b64 s[6:7], -1
	s_cbranch_scc1 .LBB1_132
	s_add_i32 s8, s10, s29
	s_ashr_i32 s9, s8, 31
	s_cmp_lt_u32 s10, 128
	s_cbranch_scc0 .Lq_glob
	s_lshl_b32 s6, s10, 9
	s_add_i32 s6, s6, 69680
	v_add_u32_e32 v8, s6, v112
	ds_read_b128 v[0:3], v8
	ds_read_b128 v[4:7], v8 offset:16
	s_branch .Lq_done

	.amdhsa_kernel _Z11edge_kernelPK15HIP_vector_typeIjLj2EEPKiPiPS_IiLj2EEPKfPK6__halfPfSD_
		.amdhsa_group_segment_fixed_size 135216
		.amdhsa_private_segment_fixed_size 0
		.amdhsa_kernarg_size 64
		.amdhsa_user_sgpr_count 2
		.amdhsa_user_sgpr_dispatch_ptr 0
		.amdhsa_user_sgpr_queue_ptr 0
		.amdhsa_user_sgpr_kernarg_segment_ptr 1
		.amdhsa_user_sgpr_dispatch_id 0
		.amdhsa_user_sgpr_kernarg_preload_length 0
		.amdhsa_user_sgpr_kernarg_preload_offset 0
		.amdhsa_user_sgpr_private_segment_size 0
		.amdhsa_uses_dynamic_stack 0
		.amdhsa_enable_private_segment 0
		.amdhsa_system_sgpr_workgroup_id_x 1
		.amdhsa_system_sgpr_workgroup_id_y 0
		.amdhsa_system_sgpr_workgroup_id_z 0
		.amdhsa_system_sgpr_workgroup_info 0
		.amdhsa_system_vgpr_workitem_id 0
		.amdhsa_next_free_vgpr 128
		.amdhsa_next_free_sgpr 44
		.amdhsa_accum_offset 128
		.amdhsa_reserve_vcc 1
		.amdhsa_float_round_mode_32 0
		.amdhsa_float_round_mode_16_64 0
		.amdhsa_float_denorm_mode_32 3
		.amdhsa_float_denorm_mode_16_64 3
		.amdhsa_dx10_clamp 1
		.amdhsa_ieee_mode 1
		.amdhsa_fp16_overflow 0
		.amdhsa_tg_split 0
		.amdhsa_exception_fp_ieee_invalid_op 0
		.amdhsa_exception_fp_denorm_src 0
		.amdhsa_exception_fp_ieee_div_zero 0
		.amdhsa_exception_fp_ieee_overflow 0
		.amdhsa_exception_fp_ieee_underflow 0
		.amdhsa_exception_fp_ieee_inexact 0
		.amdhsa_exception_int_div_zero 0
	.end_amdhsa_kernel

amdhsa.kernels:
  - .agpr_count:     0
    .args:
      - .actual_access:  read_only
        .address_space:  global
        .offset:         0
        .size:           8
        .value_kind:     global_buffer
      - .actual_access:  read_only
        .address_space:  global
        .offset:         8
        .size:           8
        .value_kind:     global_buffer
      - .actual_access:  write_only
        .address_space:  global
        .offset:         16
        .size:           8
        .value_kind:     global_buffer
      - .actual_access:  write_only
        .address_space:  global
        .offset:         24
        .size:           8
        .value_kind:     global_buffer
      - .actual_access:  write_only
        .address_space:  global
        .offset:         32
        .size:           8
        .value_kind:     global_buffer
      - .actual_access:  read_only
        .address_space:  global
        .offset:         40
        .size:           8
        .value_kind:     global_buffer
      - .actual_access:  read_only
        .address_space:  global
        .offset:         48
        .size:           8
        .value_kind:     global_buffer
      - .actual_access:  read_only
        .address_space:  global
        .offset:         56
        .size:           8
        .value_kind:     global_buffer
      - .actual_access:  read_only
        .address_space:  global
        .offset:         64
        .size:           8
        .value_kind:     global_buffer
      - .actual_access:  write_only
        .address_space:  global
        .offset:         72
        .size:           8
        .value_kind:     global_buffer
      - .actual_access:  write_only
        .address_space:  global
        .offset:         80
        .size:           8
        .value_kind:     global_buffer
    .group_segment_fixed_size: 72704
    .kernarg_segment_align: 8
    .kernarg_segment_size: 88
    .language:       OpenCL C
    .language_version:
      - 2
      - 0
    .max_flat_workgroup_size: 512
    .name:           _Z9l1_kernelPKiS0_P15HIP_vector_typeIjLj2EEPiS4_PKfS6_S6_S6_PfP6__half
    .private_segment_fixed_size: 0
    .sgpr_count:     76
    .sgpr_spill_count: 0
    .symbol:         _Z9l1_kernelPKiS0_P15HIP_vector_typeIjLj2EEPiS4_PKfS6_S6_S6_PfP6__half.kd
    .uniform_work_group_size: 1
    .uses_dynamic_stack: false
    .vgpr_count:     252
    .vgpr_spill_count: 0
    .wavefront_size: 64
  - .agpr_count:     0
    .args:
      - .actual_access:  read_only
        .address_space:  global
        .offset:         0
        .size:           8
        .value_kind:     global_buffer
      - .actual_access:  read_only
        .address_space:  global
        .offset:         8
        .size:           8
        .value_kind:     global_buffer
      - .address_space:  global
        .offset:         16
        .size:           8
        .value_kind:     global_buffer
      - .address_space:  global
        .offset:         24
        .size:           8
        .value_kind:     global_buffer
      - .actual_access:  read_only
        .address_space:  global
        .offset:         32
        .size:           8
        .value_kind:     global_buffer
      - .actual_access:  read_only
        .address_space:  global
        .offset:         40
        .size:           8
        .value_kind:     global_buffer
      - .actual_access:  write_only
        .address_space:  global
        .offset:         48
        .size:           8
        .value_kind:     global_buffer
      - .actual_access:  write_only
        .address_space:  global
        .offset:         56
        .size:           8
        .value_kind:     global_buffer
    .group_segment_fixed_size: 135216
    .kernarg_segment_align: 8
    .kernarg_segment_size: 64
    .language:       OpenCL C
    .language_version:
      - 2
      - 0
    .max_flat_workgroup_size: 1024
    .name:           _Z11edge_kernelPK15HIP_vector_typeIjLj2EEPKiPiPS_IiLj2EEPKfPK6__halfPfSD_
    .private_segment_fixed_size: 0
    .sgpr_count:     50
    .sgpr_spill_count: 0
    .symbol:         _Z11edge_kernelPK15HIP_vector_typeIjLj2EEPKiPiPS_IiLj2EEPKfPK6__halfPfSD_.kd
    .uniform_work_group_size: 1
    .uses_dynamic_stack: false
    .vgpr_count:     128
    .vgpr_spill_count: 0
    .wavefront_size: 64
